# speedup vs baseline: 1.0085x; 1.0056x over previous
_Z11head_kernelPKfS0_S0_Pf:
	s_load_dwordx4 s[4:7], s[0:1], 0x0
	s_load_dwordx2 s[2:3], s[0:1], 0x18
	s_load_dwordx2 s[10:11], s[0:1], 0x10
	v_mul_lo_u16_e32 v38, 0xcd, v0
	v_lshrrev_b16_e32 v39, 11, v38
	v_mul_i32_i24_e32 v38, -10, v39
	v_add_u32_e32 v40, v38, v0
	v_lshlrev_b32_e32 v38, 2, v40
	v_lshlrev_b32_e32 v4, 2, v0
	v_and_b32_e32 v1, 63, v0
	v_lshrrev_b32_e32 v2, 6, v0
	v_and_b32_e32 v3, 15, v1
	v_lshrrev_b32_e32 v5, 4, v1
	v_lshlrev_b32_e32 v6, 5, v2
	v_lshl_add_u32 v6, v5, 3, v6
	v_lshl_add_u32 v7, v3, 7, v6
	v_lshlrev_b32_e32 v7, 2, v7
	v_min_u32_e32 v8, 9, v3
	v_mad_u32_u24 v8, v6, 10, v8
	v_lshlrev_b32_e32 v8, 2, v8
	v_cmp_gt_u32_e64 s[12:13], 10, v3
	v_lshlrev_b32_e32 v9, 10, v2
	v_lshl_add_u32 v9, v5, 8, v9
	v_lshl_add_u32 v9, v3, 2, v9
	s_waitcnt lgkmcnt(0)
	global_load_dwordx4 v[16:19], v7, s[4:5]
	global_load_dwordx4 v[20:23], v7, s[4:5] offset:16
	global_load_dword v24, v8, s[6:7]
	global_load_dword v25, v8, s[6:7] offset:40
	global_load_dword v26, v8, s[6:7] offset:80
	global_load_dword v27, v8, s[6:7] offset:120
	global_load_dword v28, v8, s[6:7] offset:160
	global_load_dword v29, v8, s[6:7] offset:200
	global_load_dword v30, v8, s[6:7] offset:240
	global_load_dword v31, v8, s[6:7] offset:280
	global_load_dword v38, v38, s[10:11]
	s_waitcnt vmcnt(1)
	v_cndmask_b32_e64 v24, 0, v24, s[12:13]
	v_cndmask_b32_e64 v25, 0, v25, s[12:13]
	v_cndmask_b32_e64 v26, 0, v26, s[12:13]
	v_cndmask_b32_e64 v27, 0, v27, s[12:13]
	v_cndmask_b32_e64 v28, 0, v28, s[12:13]
	v_cndmask_b32_e64 v29, 0, v29, s[12:13]
	v_cndmask_b32_e64 v30, 0, v30, s[12:13]
	v_cndmask_b32_e64 v31, 0, v31, s[12:13]
	s_nop 1
	v_mfma_f32_16x16x4_f32 v[32:35], v16, v24, 0
	v_mfma_f32_16x16x4_f32 v[32:35], v17, v25, v[32:35]
	v_mfma_f32_16x16x4_f32 v[32:35], v18, v26, v[32:35]
	v_mfma_f32_16x16x4_f32 v[32:35], v19, v27, v[32:35]
	v_mfma_f32_16x16x4_f32 v[32:35], v20, v28, v[32:35]
	v_mfma_f32_16x16x4_f32 v[32:35], v21, v29, v[32:35]
	v_mfma_f32_16x16x4_f32 v[32:35], v22, v30, v[32:35]
	v_mfma_f32_16x16x4_f32 v[32:35], v23, v31, v[32:35]
	s_nop 10
	ds_write_b32 v9, v32
	ds_write_b32 v9, v33 offset:64
	ds_write_b32 v9, v34 offset:128
	ds_write_b32 v9, v35 offset:192
	s_waitcnt lgkmcnt(0)
	s_barrier
	s_movk_i32 s8, 0xa0
	v_cmp_gt_u32_e32 vcc, s8, v0
	s_and_saveexec_b64 s[4:5], vcc
	s_cbranch_execz .LBB7_4
	v_lshlrev_b32_e32 v10, 6, v39
	v_lshl_add_u32 v10, v40, 2, v10
	ds_read_b32 v11, v10
	ds_read_b32 v12, v10 offset:1024
	ds_read_b32 v13, v10 offset:2048
	ds_read_b32 v14, v10 offset:3072
	s_waitcnt vmcnt(0) lgkmcnt(0)
	v_add_f32_e32 v11, v11, v12
	v_add_f32_e32 v13, v13, v14
	v_add_f32_e32 v11, v11, v13
	v_fmamk_f32 v1, v11, 0x3b800000, v38
	ds_write_b32 v4, v1 offset:13312

	.amdhsa_kernel _Z11head_kernelPKfS0_S0_Pf
		.amdhsa_group_segment_fixed_size 13952
		.amdhsa_private_segment_fixed_size 0
		.amdhsa_kernarg_size 32
		.amdhsa_user_sgpr_count 2
		.amdhsa_user_sgpr_dispatch_ptr 0
		.amdhsa_user_sgpr_queue_ptr 0
		.amdhsa_user_sgpr_kernarg_segment_ptr 1
		.amdhsa_user_sgpr_dispatch_id 0
		.amdhsa_user_sgpr_kernarg_preload_length 0
		.amdhsa_user_sgpr_kernarg_preload_offset 0
		.amdhsa_user_sgpr_private_segment_size 0
		.amdhsa_uses_dynamic_stack 0
		.amdhsa_enable_private_segment 0
		.amdhsa_system_sgpr_workgroup_id_x 1
		.amdhsa_system_sgpr_workgroup_id_y 0
		.amdhsa_system_sgpr_workgroup_id_z 0
		.amdhsa_system_sgpr_workgroup_info 0
		.amdhsa_system_vgpr_workitem_id 0
		.amdhsa_next_free_vgpr 41
		.amdhsa_next_free_sgpr 14
		.amdhsa_accum_offset 44
		.amdhsa_reserve_vcc 1
		.amdhsa_float_round_mode_32 0
		.amdhsa_float_round_mode_16_64 0
		.amdhsa_float_denorm_mode_32 3
		.amdhsa_float_denorm_mode_16_64 3
		.amdhsa_dx10_clamp 1
		.amdhsa_ieee_mode 1
		.amdhsa_fp16_overflow 0
		.amdhsa_tg_split 0
		.amdhsa_exception_fp_ieee_invalid_op 0
		.amdhsa_exception_fp_denorm_src 0
		.amdhsa_exception_fp_ieee_div_zero 0
		.amdhsa_exception_fp_ieee_overflow 0
		.amdhsa_exception_fp_ieee_underflow 0
		.amdhsa_exception_fp_ieee_inexact 0
		.amdhsa_exception_int_div_zero 0
	.end_amdhsa_kernel

amdhsa.kernels:
  - .agpr_count:     0
    .args:
      - .offset:         0
        .size:           240
        .value_kind:     by_value
      - .actual_access:  write_only
        .address_space:  global
        .offset:         240
        .size:           8
        .value_kind:     global_buffer
      - .offset:         248
        .size:           4
        .value_kind:     hidden_block_count_x
      - .offset:         252
        .size:           4
        .value_kind:     hidden_block_count_y
      - .offset:         256
        .size:           4
        .value_kind:     hidden_block_count_z
      - .offset:         260
        .size:           2
        .value_kind:     hidden_group_size_x
      - .offset:         262
        .size:           2
        .value_kind:     hidden_group_size_y
      - .offset:         264
        .size:           2
        .value_kind:     hidden_group_size_z
      - .offset:         266
        .size:           2
        .value_kind:     hidden_remainder_x
      - .offset:         268
        .size:           2
        .value_kind:     hidden_remainder_y
      - .offset:         270
        .size:           2
        .value_kind:     hidden_remainder_z
      - .offset:         288
        .size:           8
        .value_kind:     hidden_global_offset_x
      - .offset:         296
        .size:           8
        .value_kind:     hidden_global_offset_y
      - .offset:         304
        .size:           8
        .value_kind:     hidden_global_offset_z
      - .offset:         312
        .size:           2
        .value_kind:     hidden_grid_dims
    .group_segment_fixed_size: 0
    .kernarg_segment_align: 8
    .kernarg_segment_size: 504
    .language:       OpenCL C
    .language_version:
      - 2
      - 0
    .max_flat_workgroup_size: 256
    .name:           _Z11prep_kernel8PrepArgsPc
    .private_segment_fixed_size: 0
    .sgpr_count:     50
    .sgpr_spill_count: 0
    .symbol:         _Z11prep_kernel8PrepArgsPc.kd
    .uniform_work_group_size: 1
    .uses_dynamic_stack: false
    .vgpr_count:     30
    .vgpr_spill_count: 0
    .wavefront_size: 64
  - .agpr_count:     16
    .args:
      - .actual_access:  read_only
        .address_space:  global
        .offset:         0
        .size:           8
        .value_kind:     global_buffer
      - .actual_access:  read_only
        .address_space:  global
        .offset:         8
        .size:           8
        .value_kind:     global_buffer
      - .actual_access:  read_only
        .address_space:  global
        .offset:         16
        .size:           8
        .value_kind:     global_buffer
      - .actual_access:  write_only
        .address_space:  global
        .offset:         24
        .size:           8
        .value_kind:     global_buffer
    .group_segment_fixed_size: 0
    .kernarg_segment_align: 8
    .kernarg_segment_size: 32
    .language:       OpenCL C
    .language_version:
      - 2
      - 0
    .max_flat_workgroup_size: 256
    .name:           _Z12conv1_kernelPKfPKDF16_S0_PDF16_
    .private_segment_fixed_size: 0
    .sgpr_count:     47
    .sgpr_spill_count: 0
    .symbol:         _Z12conv1_kernelPKfPKDF16_S0_PDF16_.kd
    .uniform_work_group_size: 1
    .uses_dynamic_stack: false
    .vgpr_count:     116
    .vgpr_spill_count: 0
    .wavefront_size: 64
  - .agpr_count:     32
    .args:
      - .actual_access:  read_only
        .address_space:  global
        .offset:         0
        .size:           8
        .value_kind:     global_buffer
      - .actual_access:  read_only
        .address_space:  global
        .offset:         8
        .size:           8
        .value_kind:     global_buffer
      - .actual_access:  read_only
        .address_space:  global
        .offset:         16
        .size:           8
        .value_kind:     global_buffer
      - .actual_access:  write_only
        .address_space:  global
        .offset:         24
        .size:           8
        .value_kind:     global_buffer
      - .actual_access:  write_only
        .address_space:  global
        .offset:         32
        .size:           8
        .value_kind:     global_buffer
    .group_segment_fixed_size: 0
    .kernarg_segment_align: 8
    .kernarg_segment_size: 40
    .language:       OpenCL C
    .language_version:
      - 2
      - 0
    .max_flat_workgroup_size: 64
    .name:           _Z11gat1_kernelPKDF16_S0_PKfPDF16_Pf
    .private_segment_fixed_size: 0
    .sgpr_count:     20
    .sgpr_spill_count: 0
    .symbol:         _Z11gat1_kernelPKDF16_S0_PKfPDF16_Pf.kd
    .uniform_work_group_size: 1
    .uses_dynamic_stack: false
    .vgpr_count:     284
    .vgpr_spill_count: 0
    .wavefront_size: 64
  - .agpr_count:     192
    .args:
      - .actual_access:  read_only
        .address_space:  global
        .offset:         0
        .size:           8
        .value_kind:     global_buffer
      - .actual_access:  read_only
        .address_space:  global
        .offset:         8
        .size:           8
        .value_kind:     global_buffer
      - .actual_access:  read_only
        .address_space:  global
        .offset:         16
        .size:           8
        .value_kind:     global_buffer
      - .actual_access:  read_only
        .address_space:  global
        .offset:         24
        .size:           8
        .value_kind:     global_buffer
      - .actual_access:  read_only
        .address_space:  global
        .offset:         32
        .size:           8
        .value_kind:     global_buffer
      - .actual_access:  write_only
        .address_space:  global
        .offset:         40
        .size:           8
        .value_kind:     global_buffer
      - .actual_access:  write_only
        .address_space:  global
        .offset:         48
        .size:           8
        .value_kind:     global_buffer
      - .actual_access:  read_only
        .address_space:  global
        .offset:         56
        .size:           8
        .value_kind:     global_buffer
      - .actual_access:  read_only
        .address_space:  global
        .offset:         64
        .size:           8
        .value_kind:     global_buffer
      - .actual_access:  read_only
        .address_space:  global
        .offset:         72
        .size:           8
        .value_kind:     global_buffer
      - .address_space:  global
        .offset:         80
        .size:           8
        .value_kind:     global_buffer
    .group_segment_fixed_size: 38016
    .kernarg_segment_align: 8
    .kernarg_segment_size: 88
    .language:       OpenCL C
    .language_version:
      - 2
      - 0
    .max_flat_workgroup_size: 256
    .name:           _Z11gat2_kernelPKfPKDF16_S0_S2_S0_PDF16_PfS2_S2_S0_S4_
    .private_segment_fixed_size: 0
    .sgpr_count:     22
    .sgpr_spill_count: 0
    .symbol:         _Z11gat2_kernelPKfPKDF16_S0_S2_S0_PDF16_PfS2_S2_S0_S4_.kd
    .uniform_work_group_size: 1
    .uses_dynamic_stack: false
    .vgpr_count:     424
    .vgpr_spill_count: 0
    .wavefront_size: 64
  - .agpr_count:     16
    .args:
      - .actual_access:  read_only
        .address_space:  global
        .offset:         0
        .size:           8
        .value_kind:     global_buffer
      - .actual_access:  read_only
        .address_space:  global
        .offset:         8
        .size:           8
        .value_kind:     global_buffer
      - .actual_access:  read_only
        .address_space:  global
        .offset:         16
        .size:           8
        .value_kind:     global_buffer
      - .address_space:  global
        .offset:         24
        .size:           8
        .value_kind:     global_buffer
    .group_segment_fixed_size: 1040
    .kernarg_segment_align: 8
    .kernarg_segment_size: 32
    .language:       OpenCL C
    .language_version:
      - 2
      - 0
    .max_flat_workgroup_size: 256
    .name:           _Z11gat3_kernelPKfPKDF16_S0_Pf
    .private_segment_fixed_size: 0
    .sgpr_count:     18
    .sgpr_spill_count: 0
    .symbol:         _Z11gat3_kernelPKfPKDF16_S0_Pf.kd
    .uniform_work_group_size: 1
    .uses_dynamic_stack: false
    .vgpr_count:     192
    .vgpr_spill_count: 0
    .wavefront_size: 64
  - .agpr_count:     0
    .args:
      - .actual_access:  read_only
        .address_space:  global
        .offset:         0
        .size:           8
        .value_kind:     global_buffer
      - .actual_access:  read_only
        .address_space:  global
        .offset:         8
        .size:           8
        .value_kind:     global_buffer
      - .actual_access:  read_only
        .address_space:  global
        .offset:         16
        .size:           8
        .value_kind:     global_buffer
      - .actual_access:  read_only
        .address_space:  global
        .offset:         24
        .size:           8
        .value_kind:     global_buffer
      - .actual_access:  read_only
        .address_space:  global
        .offset:         32
        .size:           8
        .value_kind:     global_buffer
      - .actual_access:  read_only
        .address_space:  global
        .offset:         40
        .size:           8
        .value_kind:     global_buffer
      - .actual_access:  write_only
        .address_space:  global
        .offset:         48
        .size:           8
        .value_kind:     global_buffer
    .group_segment_fixed_size: 87680
    .kernarg_segment_align: 8
    .kernarg_segment_size: 56
    .language:       OpenCL C
    .language_version:
      - 2
      - 0
    .max_flat_workgroup_size: 512
    .name:           _Z12gat3p_kernelPKfPKDF16_S0_S0_S0_S0_Pf
    .private_segment_fixed_size: 0
    .sgpr_count:     78
    .sgpr_spill_count: 0
    .symbol:         _Z12gat3p_kernelPKfPKDF16_S0_S0_S0_S0_Pf.kd
    .uniform_work_group_size: 1
    .uses_dynamic_stack: false
    .vgpr_count:     206
    .vgpr_spill_count: 0
    .wavefront_size: 64
  - .agpr_count:     0
    .args:
      - .actual_access:  read_only
        .address_space:  global
        .offset:         0
        .size:           8
        .value_kind:     global_buffer
      - .actual_access:  read_only
        .address_space:  global
        .offset:         8
        .size:           8
        .value_kind:     global_buffer
      - .actual_access:  read_only
        .address_space:  global
        .offset:         16
        .size:           8
        .value_kind:     global_buffer
      - .address_space:  global
        .offset:         24
        .size:           8
        .value_kind:     global_buffer
    .group_segment_fixed_size: 2048
    .kernarg_segment_align: 8
    .kernarg_segment_size: 32
    .language:       OpenCL C
    .language_version:
      - 2
      - 0
    .max_flat_workgroup_size: 64
    .name:           _Z12gat3s_kernelPKfPKDF16_S0_Pf
    .private_segment_fixed_size: 0
    .sgpr_count:     26
    .sgpr_spill_count: 0
    .symbol:         _Z12gat3s_kernelPKfPKDF16_S0_Pf.kd
    .uniform_work_group_size: 1
    .uses_dynamic_stack: false
    .vgpr_count:     192
    .vgpr_spill_count: 0
    .wavefront_size: 64
  - .agpr_count:     0
    .args:
      - .actual_access:  read_only
        .address_space:  global
        .offset:         0
        .size:           8
        .value_kind:     global_buffer
      - .actual_access:  read_only
        .address_space:  global
        .offset:         8
        .size:           8
        .value_kind:     global_buffer
      - .actual_access:  read_only
        .address_space:  global
        .offset:         16
        .size:           8
        .value_kind:     global_buffer
      - .actual_access:  write_only
        .address_space:  global
        .offset:         24
        .size:           8
        .value_kind:     global_buffer
    .group_segment_fixed_size: 13952
    .kernarg_segment_align: 8
    .kernarg_segment_size: 32
    .language:       OpenCL C
    .language_version:
      - 2
      - 0
    .max_flat_workgroup_size: 256
    .name:           _Z11head_kernelPKfS0_S0_Pf
    .private_segment_fixed_size: 0
    .sgpr_count:     15
    .sgpr_spill_count: 0
    .symbol:         _Z11head_kernelPKfS0_S0_Pf.kd
    .uniform_work_group_size: 1
    .uses_dynamic_stack: false
    .vgpr_count:     41
    .vgpr_spill_count: 0
    .wavefront_size: 64
  - .agpr_count:     0
    .args:
      - .actual_access:  read_only
        .address_space:  global
        .offset:         0
        .size:           8
        .value_kind:     global_buffer
      - .actual_access:  read_only
        .address_space:  global
        .offset:         8
        .size:           8
        .value_kind:     global_buffer
      - .actual_access:  read_only
        .address_space:  global
        .offset:         16
        .size:           8
        .value_kind:     global_buffer
      - .actual_access:  write_only
        .address_space:  global
        .offset:         24
        .size:           8
        .value_kind:     global_buffer
    .group_segment_fixed_size: 640
    .kernarg_segment_align: 8
    .kernarg_segment_size: 32
    .language:       OpenCL C
    .language_version:
      - 2
      - 0
    .max_flat_workgroup_size: 256
    .name:           _Z12final_kernelPKfS0_S0_Pf
    .private_segment_fixed_size: 0
    .sgpr_count:     18
    .sgpr_spill_count: 0
    .symbol:         _Z12final_kernelPKfS0_S0_Pf.kd
    .uniform_work_group_size: 1
    .uses_dynamic_stack: false
    .vgpr_count:     37
    .vgpr_spill_count: 0
    .wavefront_size: 64
  - .agpr_count:     0
    .args:
      - .actual_access:  read_only
        .address_space:  global
        .offset:         0
        .size:           8
        .value_kind:     global_buffer
      - .address_space:  global
        .offset:         8
        .size:           8
        .value_kind:     global_buffer
      - .actual_access:  read_only
        .address_space:  global
        .offset:         16
        .size:           8
        .value_kind:     global_buffer
      - .actual_access:  write_only
        .address_space:  global
        .offset:         24
        .size:           8
        .value_kind:     global_buffer
      - .actual_access:  read_only
        .address_space:  global
        .offset:         32
        .size:           8
        .value_kind:     global_buffer
      - .actual_access:  read_only
        .address_space:  global
        .offset:         40
        .size:           8
        .value_kind:     global_buffer
      - .actual_access:  read_only
        .address_space:  global
        .offset:         48
        .size:           8
        .value_kind:     global_buffer
      - .actual_access:  read_only
        .address_space:  global
        .offset:         56
        .size:           8
        .value_kind:     global_buffer
      - .offset:         64
        .size:           4
        .value_kind:     hidden_block_count_x
      - .offset:         68
        .size:           4
        .value_kind:     hidden_block_count_y
      - .offset:         72
        .size:           4
        .value_kind:     hidden_block_count_z
      - .offset:         76
        .size:           2
        .value_kind:     hidden_group_size_x
      - .offset:         78
        .size:           2
        .value_kind:     hidden_group_size_y
      - .offset:         80
        .size:           2
        .value_kind:     hidden_group_size_z
      - .offset:         82
        .size:           2
        .value_kind:     hidden_remainder_x
      - .offset:         84
        .size:           2
        .value_kind:     hidden_remainder_y
      - .offset:         86
        .size:           2
        .value_kind:     hidden_remainder_z
      - .offset:         104
        .size:           8
        .value_kind:     hidden_global_offset_x
      - .offset:         112
        .size:           8
        .value_kind:     hidden_global_offset_y
      - .offset:         120
        .size:           8
        .value_kind:     hidden_global_offset_z
      - .offset:         128
        .size:           2
        .value_kind:     hidden_grid_dims
    .group_segment_fixed_size: 74240
    .kernarg_segment_align: 8
    .kernarg_segment_size: 320
    .language:       OpenCL C
    .language_version:
      - 2
      - 0
    .max_flat_workgroup_size: 256
    .name:           _Z11conv_kernelILi64ELi128ELi128ELi128ELi4ELi2ELi2ELb1ELi1ELb0ELb0ELi2EEvPKDF16_S1_PKfPDF16_S1_S3_S1_S3_
    .private_segment_fixed_size: 0
    .sgpr_count:     58
    .sgpr_spill_count: 0
    .symbol:         _Z11conv_kernelILi64ELi128ELi128ELi128ELi4ELi2ELi2ELb1ELi1ELb0ELb0ELi2EEvPKDF16_S1_PKfPDF16_S1_S3_S1_S3_.kd
    .uniform_work_group_size: 1
    .uses_dynamic_stack: false
    .vgpr_count:     256
    .vgpr_spill_count: 0
    .wavefront_size: 64
  - .agpr_count:     0
    .args:
      - .address_space:  global
        .offset:         0
        .size:           8
        .value_kind:     global_buffer
      - .address_space:  global
        .offset:         8
        .size:           8
        .value_kind:     global_buffer
      - .actual_access:  read_only
        .address_space:  global
        .offset:         16
        .size:           8
        .value_kind:     global_buffer
      - .actual_access:  write_only
        .address_space:  global
        .offset:         24
        .size:           8
        .value_kind:     global_buffer
      - .address_space:  global
        .offset:         32
        .size:           8
        .value_kind:     global_buffer
      - .actual_access:  read_only
        .address_space:  global
        .offset:         40
        .size:           8
        .value_kind:     global_buffer
      - .actual_access:  read_only
        .address_space:  global
        .offset:         48
        .size:           8
        .value_kind:     global_buffer
      - .actual_access:  read_only
        .address_space:  global
        .offset:         56
        .size:           8
        .value_kind:     global_buffer
      - .offset:         64
        .size:           4
        .value_kind:     hidden_block_count_x
      - .offset:         68
        .size:           4
        .value_kind:     hidden_block_count_y
      - .offset:         72
        .size:           4
        .value_kind:     hidden_block_count_z
      - .offset:         76
        .size:           2
        .value_kind:     hidden_group_size_x
      - .offset:         78
        .size:           2
        .value_kind:     hidden_group_size_y
      - .offset:         80
        .size:           2
        .value_kind:     hidden_group_size_z
      - .offset:         82
        .size:           2
        .value_kind:     hidden_remainder_x
      - .offset:         84
        .size:           2
        .value_kind:     hidden_remainder_y
      - .offset:         86
        .size:           2
        .value_kind:     hidden_remainder_z
      - .offset:         104
        .size:           8
        .value_kind:     hidden_global_offset_x
      - .offset:         112
        .size:           8
        .value_kind:     hidden_global_offset_y
      - .offset:         120
        .size:           8
        .value_kind:     hidden_global_offset_z
      - .offset:         128
        .size:           2
        .value_kind:     hidden_grid_dims
    .group_segment_fixed_size: 148480
    .kernarg_segment_align: 8
    .kernarg_segment_size: 320
    .language:       OpenCL C
    .language_version:
      - 2
      - 0
    .max_flat_workgroup_size: 512
    .name:           _Z11conv_kernelILi128ELi256ELi64ELi64ELi4ELi2ELi4ELb0ELi1ELb1ELb0ELi1EEvPKDF16_S1_PKfPDF16_S1_S3_S1_S3_
    .private_segment_fixed_size: 0
    .sgpr_count:     28
    .sgpr_spill_count: 0
    .symbol:         _Z11conv_kernelILi128ELi256ELi64ELi64ELi4ELi2ELi4ELb0ELi1ELb1ELb0ELi1EEvPKDF16_S1_PKfPDF16_S1_S3_S1_S3_.kd
    .uniform_work_group_size: 1
    .uses_dynamic_stack: false
    .vgpr_count:     234
    .vgpr_spill_count: 0
    .wavefront_size: 64
  - .agpr_count:     0
    .args:
      - .address_space:  global
        .offset:         0
        .size:           8
        .value_kind:     global_buffer
      - .address_space:  global
        .offset:         8
        .size:           8
        .value_kind:     global_buffer
      - .actual_access:  read_only
        .address_space:  global
        .offset:         16
        .size:           8
        .value_kind:     global_buffer
      - .actual_access:  write_only
        .address_space:  global
        .offset:         24
        .size:           8
        .value_kind:     global_buffer
      - .address_space:  global
        .offset:         32
        .size:           8
        .value_kind:     global_buffer
      - .actual_access:  read_only
        .address_space:  global
        .offset:         40
        .size:           8
        .value_kind:     global_buffer
      - .actual_access:  read_only
        .address_space:  global
        .offset:         48
        .size:           8
        .value_kind:     global_buffer
      - .actual_access:  read_only
        .address_space:  global
        .offset:         56
        .size:           8
        .value_kind:     global_buffer
      - .offset:         64
        .size:           4
        .value_kind:     hidden_block_count_x
      - .offset:         68
        .size:           4
        .value_kind:     hidden_block_count_y
      - .offset:         72
        .size:           4
        .value_kind:     hidden_block_count_z
      - .offset:         76
        .size:           2
        .value_kind:     hidden_group_size_x
      - .offset:         78
        .size:           2
        .value_kind:     hidden_group_size_y
      - .offset:         80
        .size:           2
        .value_kind:     hidden_group_size_z
      - .offset:         82
        .size:           2
        .value_kind:     hidden_remainder_x
      - .offset:         84
        .size:           2
        .value_kind:     hidden_remainder_y
      - .offset:         86
        .size:           2
        .value_kind:     hidden_remainder_z
      - .offset:         104
        .size:           8
        .value_kind:     hidden_global_offset_x
      - .offset:         112
        .size:           8
        .value_kind:     hidden_global_offset_y
      - .offset:         120
        .size:           8
        .value_kind:     hidden_global_offset_z
      - .offset:         128
        .size:           2
        .value_kind:     hidden_grid_dims
    .group_segment_fixed_size: 157696
    .kernarg_segment_align: 8
    .kernarg_segment_size: 320
    .language:       OpenCL C
    .language_version:
      - 2
      - 0
    .max_flat_workgroup_size: 512
    .name:           _Z11conv_kernelILi256ELi256ELi32ELi32ELi2ELi2ELi2ELb0ELi2ELb0ELb1ELi1EEvPKDF16_S1_PKfPDF16_S1_S3_S1_S3_
    .private_segment_fixed_size: 0
    .sgpr_count:     30
    .sgpr_spill_count: 0
    .symbol:         _Z11conv_kernelILi256ELi256ELi32ELi32ELi2ELi2ELi2ELb0ELi2ELb0ELb1ELi1EEvPKDF16_S1_PKfPDF16_S1_S3_S1_S3_.kd
    .uniform_work_group_size: 1
    .uses_dynamic_stack: false
    .vgpr_count:     121
    .vgpr_spill_count: 0
    .wavefront_size: 64
